# MoE GEMM 2: half the workgroups start the phase ~8 us later so that the halves' epilogue store bursts interleave with the other half's K loops
# baseline (speedup 1.0000x reference)
.LBB0_1852:
	s_bitcmp1_b32 s2, 3
	s_cbranch_scc0 .Lstag2_skip
	s_sleep 127
	s_sleep 127
